# k_agg1: when every active node of the wave has at most 4 neighbours left, the final step gathers 4 rows instead of 8 (same packed-fp16 tree, pad half omitted)
# speedup vs baseline: 1.0096x; 1.0096x over previous
.LBB3_4:
	v_sub_u32_e32 v62, v1, v0
	v_cmp_lt_i32_e64 s[18:19], 4, v62
	s_cmp_eq_u64 s[18:19], 0
	s_cbranch_scc1 .Lagg_four
	global_load_dwordx4 v[30:33], v[2:3], off
	v_add_u32_e32 v0, 8, v0
	v_cmp_ge_i32_e64 s[18:19], v0, v1
	v_lshl_add_u64 v[2:3], v[2:3], 0, 16
	s_or_b64 s[30:31], s[18:19], s[30:31]
	s_waitcnt vmcnt(0)
	v_lshlrev_b32_sdwa v34, v28, v30 dst_sel:DWORD dst_unused:UNUSED_PAD src0_sel:DWORD src1_sel:WORD_1
	v_lshlrev_b32_sdwa v30, v28, v30 dst_sel:DWORD dst_unused:UNUSED_PAD src0_sel:DWORD src1_sel:WORD_0
	v_lshlrev_b32_sdwa v35, v28, v31 dst_sel:DWORD dst_unused:UNUSED_PAD src0_sel:DWORD src1_sel:WORD_1
	v_lshlrev_b32_sdwa v31, v28, v31 dst_sel:DWORD dst_unused:UNUSED_PAD src0_sel:DWORD src1_sel:WORD_0
	v_lshlrev_b32_sdwa v36, v28, v32 dst_sel:DWORD dst_unused:UNUSED_PAD src0_sel:DWORD src1_sel:WORD_1
	v_lshlrev_b32_sdwa v32, v28, v32 dst_sel:DWORD dst_unused:UNUSED_PAD src0_sel:DWORD src1_sel:WORD_0
	v_lshlrev_b32_sdwa v37, v28, v33 dst_sel:DWORD dst_unused:UNUSED_PAD src0_sel:DWORD src1_sel:WORD_1
	v_lshlrev_b32_sdwa v33, v28, v33 dst_sel:DWORD dst_unused:UNUSED_PAD src0_sel:DWORD src1_sel:WORD_0
	v_or_b32_e32 v38, v34, v7
	v_or_b32_e32 v39, v30, v6
	v_or_b32_e32 v42, v35, v7
	v_or_b32_e32 v40, v31, v6
	v_or_b32_e32 v50, v36, v7
	v_or_b32_e32 v46, v32, v6
	v_or_b32_e32 v58, v37, v7
	v_or_b32_e32 v54, v33, v6
	global_load_dwordx4 v[30:33], v39, s[20:21]
	global_load_dwordx4 v[34:37], v38, s[20:21]
	s_nop 0
	global_load_dwordx4 v[38:41], v40, s[20:21]
	s_nop 0
	global_load_dwordx4 v[42:45], v42, s[20:21]
	s_nop 0
	global_load_dwordx4 v[46:49], v46, s[20:21]
	s_nop 0
	global_load_dwordx4 v[50:53], v50, s[20:21]
	s_nop 0
	global_load_dwordx4 v[54:57], v54, s[20:21]
	s_nop 0
	global_load_dwordx4 v[58:61], v58, s[20:21]
	s_waitcnt vmcnt(6)
	v_pk_add_f16 v33, v33, v37
	v_pk_add_f16 v32, v32, v36
	v_pk_add_f16 v31, v31, v35
	v_pk_add_f16 v30, v30, v34
	s_waitcnt vmcnt(4)
	v_pk_add_f16 v34, v41, v45
	v_pk_add_f16 v35, v40, v44
	v_pk_add_f16 v36, v39, v43
	v_pk_add_f16 v37, v38, v42
	s_waitcnt vmcnt(2)
	v_pk_add_f16 v38, v49, v53
	v_pk_add_f16 v39, v48, v52
	v_pk_add_f16 v40, v47, v51
	v_pk_add_f16 v41, v46, v50
	s_waitcnt vmcnt(0)
	v_pk_add_f16 v42, v57, v61
	v_pk_add_f16 v43, v56, v60
	v_pk_add_f16 v44, v55, v59
	v_pk_add_f16 v45, v54, v58
	v_pk_add_f16 v30, v30, v37
	v_pk_add_f16 v31, v31, v36
	v_pk_add_f16 v32, v32, v35
	v_pk_add_f16 v33, v33, v34
	v_pk_add_f16 v34, v41, v45
	v_pk_add_f16 v35, v40, v44
	v_pk_add_f16 v36, v39, v43
	v_pk_add_f16 v37, v38, v42
	v_pk_add_f16 v36, v32, v36
	v_pk_add_f16 v37, v33, v37
	v_pk_add_f16 v33, v31, v35
	v_pk_add_f16 v31, v30, v34
	v_cvt_f32_f16_e32 v32, v33
	v_cvt_f32_f16_e32 v30, v31
	v_cvt_f32_f16_sdwa v31, v31 dst_sel:DWORD dst_unused:UNUSED_PAD src0_sel:WORD_1
	v_cvt_f32_f16_sdwa v33, v33 dst_sel:DWORD dst_unused:UNUSED_PAD src0_sel:WORD_1
	v_cvt_f32_f16_e32 v34, v36
	v_cvt_f32_f16_sdwa v35, v36 dst_sel:DWORD dst_unused:UNUSED_PAD src0_sel:WORD_1
	v_cvt_f32_f16_e32 v36, v37
	v_cvt_f32_f16_sdwa v37, v37 dst_sel:DWORD dst_unused:UNUSED_PAD src0_sel:WORD_1
	v_pk_add_f32 v[18:19], v[18:19], v[30:31]
	v_pk_add_f32 v[16:17], v[16:17], v[32:33]
	v_pk_add_f32 v[14:15], v[14:15], v[34:35]
	v_pk_add_f32 v[12:13], v[12:13], v[36:37]
	s_andn2_b64 exec, exec, s[30:31]
	s_cbranch_execnz .LBB3_4
	s_branch .Lagg_loop_done
.Lagg_four:
	global_load_dwordx2 v[30:31], v[2:3], off
	s_waitcnt vmcnt(0)
	v_lshlrev_b32_sdwa v34, v28, v30 dst_sel:DWORD dst_unused:UNUSED_PAD src0_sel:DWORD src1_sel:WORD_1
	v_lshlrev_b32_sdwa v30, v28, v30 dst_sel:DWORD dst_unused:UNUSED_PAD src0_sel:DWORD src1_sel:WORD_0
	v_lshlrev_b32_sdwa v35, v28, v31 dst_sel:DWORD dst_unused:UNUSED_PAD src0_sel:DWORD src1_sel:WORD_1
	v_lshlrev_b32_sdwa v31, v28, v31 dst_sel:DWORD dst_unused:UNUSED_PAD src0_sel:DWORD src1_sel:WORD_0
	v_or_b32_e32 v38, v34, v7
	v_or_b32_e32 v39, v30, v6
	v_or_b32_e32 v42, v35, v7
	v_or_b32_e32 v40, v31, v6
	global_load_dwordx4 v[30:33], v39, s[20:21]
	global_load_dwordx4 v[34:37], v38, s[20:21]
	s_nop 0
	global_load_dwordx4 v[38:41], v40, s[20:21]
	s_nop 0
	global_load_dwordx4 v[42:45], v42, s[20:21]
	s_waitcnt vmcnt(2)
	v_pk_add_f16 v33, v33, v37
	v_pk_add_f16 v32, v32, v36
	v_pk_add_f16 v31, v31, v35
	v_pk_add_f16 v30, v30, v34
	s_waitcnt vmcnt(0)
	v_pk_add_f16 v34, v41, v45
	v_pk_add_f16 v35, v40, v44
	v_pk_add_f16 v36, v39, v43
	v_pk_add_f16 v37, v38, v42
	v_pk_add_f16 v30, v30, v37
	v_pk_add_f16 v31, v31, v36
	v_pk_add_f16 v32, v32, v35
	v_pk_add_f16 v33, v33, v34
	v_cvt_f32_f16_e32 v34, v30
	v_cvt_f32_f16_sdwa v35, v30 dst_sel:DWORD dst_unused:UNUSED_PAD src0_sel:WORD_1
	v_cvt_f32_f16_e32 v36, v31
	v_cvt_f32_f16_sdwa v37, v31 dst_sel:DWORD dst_unused:UNUSED_PAD src0_sel:WORD_1
	v_cvt_f32_f16_e32 v38, v32
	v_cvt_f32_f16_sdwa v39, v32 dst_sel:DWORD dst_unused:UNUSED_PAD src0_sel:WORD_1
	v_cvt_f32_f16_e32 v40, v33
	v_cvt_f32_f16_sdwa v41, v33 dst_sel:DWORD dst_unused:UNUSED_PAD src0_sel:WORD_1
	v_pk_add_f32 v[18:19], v[18:19], v[34:35]
	v_pk_add_f32 v[16:17], v[16:17], v[36:37]
	v_pk_add_f32 v[14:15], v[14:15], v[38:39]
	v_pk_add_f32 v[12:13], v[12:13], v[40:41]
.Lagg_loop_done:
	s_or_b64 exec, exec, s[30:31]

	.amdhsa_kernel _Z6k_agg1PKDF16_PK15HIP_vector_typeIiLj2EEPKtPKfS8_S8_Pf
		.amdhsa_group_segment_fixed_size 2304
		.amdhsa_private_segment_fixed_size 0
		.amdhsa_kernarg_size 56
		.amdhsa_user_sgpr_count 2
		.amdhsa_user_sgpr_dispatch_ptr 0
		.amdhsa_user_sgpr_queue_ptr 0
		.amdhsa_user_sgpr_kernarg_segment_ptr 1
		.amdhsa_user_sgpr_dispatch_id 0
		.amdhsa_user_sgpr_kernarg_preload_length 0
		.amdhsa_user_sgpr_kernarg_preload_offset 0
		.amdhsa_user_sgpr_private_segment_size 0
		.amdhsa_uses_dynamic_stack 0
		.amdhsa_enable_private_segment 0
		.amdhsa_system_sgpr_workgroup_id_x 1
		.amdhsa_system_sgpr_workgroup_id_y 0
		.amdhsa_system_sgpr_workgroup_id_z 0
		.amdhsa_system_sgpr_workgroup_info 0
		.amdhsa_system_vgpr_workitem_id 0
		.amdhsa_next_free_vgpr 63
		.amdhsa_next_free_sgpr 34
		.amdhsa_accum_offset 64
		.amdhsa_reserve_vcc 1
		.amdhsa_float_round_mode_32 0
		.amdhsa_float_round_mode_16_64 0
		.amdhsa_float_denorm_mode_32 3
		.amdhsa_float_denorm_mode_16_64 3
		.amdhsa_dx10_clamp 1
		.amdhsa_ieee_mode 1
		.amdhsa_fp16_overflow 0
		.amdhsa_tg_split 0
		.amdhsa_exception_fp_ieee_invalid_op 0
		.amdhsa_exception_fp_denorm_src 0
		.amdhsa_exception_fp_ieee_div_zero 0
		.amdhsa_exception_fp_ieee_overflow 0
		.amdhsa_exception_fp_ieee_underflow 0
		.amdhsa_exception_fp_ieee_inexact 0
		.amdhsa_exception_int_div_zero 0
	.end_amdhsa_kernel

amdhsa.kernels:
  - .agpr_count:     0
    .args:
      - .actual_access:  read_only
        .address_space:  global
        .offset:         0
        .size:           8
        .value_kind:     global_buffer
      - .actual_access:  write_only
        .address_space:  global
        .offset:         8
        .size:           8
        .value_kind:     global_buffer
      - .actual_access:  write_only
        .address_space:  global
        .offset:         16
        .size:           8
        .value_kind:     global_buffer
      - .actual_access:  read_only
        .address_space:  global
        .offset:         24
        .size:           8
        .value_kind:     global_buffer
      - .actual_access:  write_only
        .address_space:  global
        .offset:         32
        .size:           8
        .value_kind:     global_buffer
      - .actual_access:  write_only
        .address_space:  global
        .offset:         40
        .size:           8
        .value_kind:     global_buffer
    .group_segment_fixed_size: 14576
    .kernarg_segment_align: 8
    .kernarg_segment_size: 48
    .language:       OpenCL C
    .language_version:
      - 2
      - 0
    .max_flat_workgroup_size: 256
    .name:           _Z5k_binPKiPiPjPKfPDv8_DF16_PDF16_
    .private_segment_fixed_size: 0
    .sgpr_count:     22
    .sgpr_spill_count: 0
    .symbol:         _Z5k_binPKiPiPjPKfPDv8_DF16_PDF16_.kd
    .uniform_work_group_size: 1
    .uses_dynamic_stack: false
    .vgpr_count:     75
    .vgpr_spill_count: 0
    .wavefront_size: 64
  - .agpr_count:     0
    .args:
      - .actual_access:  read_only
        .address_space:  global
        .offset:         0
        .size:           8
        .value_kind:     global_buffer
      - .actual_access:  read_only
        .address_space:  global
        .offset:         8
        .size:           8
        .value_kind:     global_buffer
      - .actual_access:  write_only
        .address_space:  global
        .offset:         16
        .size:           8
        .value_kind:     global_buffer
      - .actual_access:  write_only
        .address_space:  global
        .offset:         24
        .size:           8
        .value_kind:     global_buffer
      - .actual_access:  write_only
        .address_space:  global
        .offset:         32
        .size:           8
        .value_kind:     global_buffer
      - .actual_access:  write_only
        .address_space:  global
        .offset:         40
        .size:           8
        .value_kind:     global_buffer
    .group_segment_fixed_size: 18452
    .kernarg_segment_align: 8
    .kernarg_segment_size: 48
    .language:       OpenCL C
    .language_version:
      - 2
      - 0
    .max_flat_workgroup_size: 256
    .name:           _Z5k_csrPKiPKjP15HIP_vector_typeIiLj2EEPfPtS6_
    .private_segment_fixed_size: 0
    .sgpr_count:     94
    .sgpr_spill_count: 0
    .symbol:         _Z5k_csrPKiPKjP15HIP_vector_typeIiLj2EEPfPtS6_.kd
    .uniform_work_group_size: 1
    .uses_dynamic_stack: false
    .vgpr_count:     65
    .vgpr_spill_count: 0
    .wavefront_size: 64
  - .agpr_count:     0
    .args:
      - .actual_access:  read_only
        .address_space:  global
        .offset:         0
        .size:           8
        .value_kind:     global_buffer
      - .actual_access:  read_only
        .address_space:  global
        .offset:         8
        .size:           8
        .value_kind:     global_buffer
      - .actual_access:  read_only
        .address_space:  global
        .offset:         16
        .size:           8
        .value_kind:     global_buffer
      - .actual_access:  read_only
        .address_space:  global
        .offset:         24
        .size:           8
        .value_kind:     global_buffer
      - .actual_access:  write_only
        .address_space:  global
        .offset:         32
        .size:           8
        .value_kind:     global_buffer
    .group_segment_fixed_size: 129152
    .kernarg_segment_align: 8
    .kernarg_segment_size: 40
    .language:       OpenCL C
    .language_version:
      - 2
      - 0
    .max_flat_workgroup_size: 512
    .name:           _Z6k_gemmPKfPKDv8_DF16_S0_S0_PDF16_
    .private_segment_fixed_size: 0
    .sgpr_count:     22
    .sgpr_spill_count: 0
    .symbol:         _Z6k_gemmPKfPKDv8_DF16_S0_S0_PDF16_.kd
    .uniform_work_group_size: 1
    .uses_dynamic_stack: false
    .vgpr_count:     256
    .vgpr_spill_count: 0
    .wavefront_size: 64
  - .agpr_count:     0
    .args:
      - .actual_access:  read_only
        .address_space:  global
        .offset:         0
        .size:           8
        .value_kind:     global_buffer
      - .actual_access:  read_only
        .address_space:  global
        .offset:         8
        .size:           8
        .value_kind:     global_buffer
      - .actual_access:  read_only
        .address_space:  global
        .offset:         16
        .size:           8
        .value_kind:     global_buffer
      - .actual_access:  read_only
        .address_space:  global
        .offset:         24
        .size:           8
        .value_kind:     global_buffer
      - .actual_access:  read_only
        .address_space:  global
        .offset:         32
        .size:           8
        .value_kind:     global_buffer
      - .actual_access:  read_only
        .address_space:  global
        .offset:         40
        .size:           8
        .value_kind:     global_buffer
      - .address_space:  global
        .offset:         48
        .size:           8
        .value_kind:     global_buffer
    .group_segment_fixed_size: 2304
    .kernarg_segment_align: 8
    .kernarg_segment_size: 56
    .language:       OpenCL C
    .language_version:
      - 2
      - 0
    .max_flat_workgroup_size: 320
    .name:           _Z6k_agg1PKDF16_PK15HIP_vector_typeIiLj2EEPKtPKfS8_S8_Pf
    .private_segment_fixed_size: 0
    .sgpr_count:     40
    .sgpr_spill_count: 0
    .symbol:         _Z6k_agg1PKDF16_PK15HIP_vector_typeIiLj2EEPKtPKfS8_S8_Pf.kd
    .uniform_work_group_size: 1
    .uses_dynamic_stack: false
    .vgpr_count:     63
    .vgpr_spill_count: 0
    .wavefront_size: 64
  - .agpr_count:     0
    .args:
      - .actual_access:  read_only
        .address_space:  global
        .offset:         0
        .size:           8
        .value_kind:     global_buffer
      - .actual_access:  read_only
        .address_space:  global
        .offset:         8
        .size:           8
        .value_kind:     global_buffer
      - .actual_access:  read_only
        .address_space:  global
        .offset:         16
        .size:           8
        .value_kind:     global_buffer
      - .actual_access:  read_only
        .address_space:  global
        .offset:         24
        .size:           8
        .value_kind:     global_buffer
      - .actual_access:  read_only
        .address_space:  global
        .offset:         32
        .size:           8
        .value_kind:     global_buffer
      - .actual_access:  write_only
        .address_space:  global
        .offset:         40
        .size:           8
        .value_kind:     global_buffer
    .group_segment_fixed_size: 0
    .kernarg_segment_align: 8
    .kernarg_segment_size: 48
    .language:       OpenCL C
    .language_version:
      - 2
      - 0
    .max_flat_workgroup_size: 256
    .name:           _Z5k_outPKfPK15HIP_vector_typeIiLj2EEPKtS0_S0_Pf
    .private_segment_fixed_size: 0
    .sgpr_count:     18
    .sgpr_spill_count: 0
    .symbol:         _Z5k_outPKfPK15HIP_vector_typeIiLj2EEPKtS0_S0_Pf.kd
    .uniform_work_group_size: 1
    .uses_dynamic_stack: false
    .vgpr_count:     27
    .vgpr_spill_count: 0
    .wavefront_size: 64
